# P7 top-k butterflies fused into v_max/v_add with DPP source operands and permlane swaps (fewer VALU ops per reduction step)
# speedup vs baseline: 1.0121x; 1.0121x over previous
.LBB0_1143:
	s_mov_b32 s98, 0xffff0000
	s_mov_b32 s99, 0xffff0000
	s_mov_b32 s100, 0
	s_mov_b32 s101, -1
	s_or_b32 s74, s16, s62
	v_lshl_add_u32 v66, s74, 8, v194
	ds_read2st64_b32 v[66:67], v66 offset1:16
	s_waitcnt lgkmcnt(0)
	v_add_f32_e32 v66, v66, v67
	v_mul_f32_e32 v67, 0xbfb8aa3b, v66
	v_fma_f32 v68, v66, s70, -v67
	v_rndne_f32_e32 v69, v67
	v_fmac_f32_e32 v68, 0xb2a5705f, v66
	v_sub_f32_e32 v67, v67, v69
	v_add_f32_e32 v67, v67, v68
	v_exp_f32_e32 v67, v67
	v_cvt_i32_f32_e32 v68, v69
	v_cmp_nlt_f32_e32 vcc, s71, v66
	v_ldexp_f32 v67, v67, v68
	s_nop 0
	v_cndmask_b32_e32 v67, 0, v67, vcc
	v_cmp_ngt_f32_e32 vcc, s72, v66
	s_nop 1
	v_cndmask_b32_e32 v66, v204, v67, vcc
	v_add_f32_e32 v66, 1.0, v66
	v_div_scale_f32 v67, s[16:17], v66, v66, 1.0
	v_rcp_f32_e32 v68, v67
	s_nop 0
	v_fma_f32 v69, -v67, v68, 1.0
	v_fmac_f32_e32 v68, v69, v68
	v_div_scale_f32 v69, vcc, 1.0, v66, 1.0
	v_mul_f32_e32 v70, v69, v68
	v_fma_f32 v71, -v67, v70, v69
	v_fmac_f32_e32 v70, v71, v68
	v_fma_f32 v67, -v67, v70, v69
	v_div_fmas_f32 v67, v67, v68, v70
	v_div_fixup_f32 v66, v67, v66, 1.0
	v_mov_b32_e32 v67, v240
	v_add_f32_e32 v67, v67, v66
	s_nop 1
	v_max_f32_dpp v68, v67, v67 quad_perm:[1,0,3,2] row_mask:0xf bank_mask:0xf
	s_nop 1
	v_max_f32_dpp v68, v68, v68 quad_perm:[2,3,0,1] row_mask:0xf bank_mask:0xf
	s_nop 1
	v_max_f32_dpp v70, v68, v68 row_half_mirror row_mask:0xf bank_mask:0xf
	v_cmp_eq_f32_e32 vcc, v67, v70
	s_nop 1
	v_and_b32_e32 v69, vcc_hi, v87
	v_and_b32_e32 v68, vcc_lo, v86
	v_cmp_ne_u64_e32 vcc, 0, v[68:69]
	v_ffbl_b32_e32 v69, v69
	v_add_u32_e32 v69, 32, v69
	v_ffbl_b32_e32 v68, v68
	v_min_u32_e32 v68, v68, v69
	v_cmp_eq_u32_e64 s[16:17], v206, v68
	s_and_b64 vcc, vcc, s[16:17]
	v_cndmask_b32_e32 v68, v67, v205, vcc
	s_nop 1
	v_max_f32_dpp v68, v68, v68 quad_perm:[1,0,3,2] row_mask:0xf bank_mask:0xf
	s_nop 1
	v_max_f32_dpp v68, v68, v68 quad_perm:[2,3,0,1] row_mask:0xf bank_mask:0xf
	s_nop 1
	v_max_f32_dpp v68, v68, v68 row_half_mirror row_mask:0xf bank_mask:0xf
	v_add_f32_e32 v68, v70, v68
	s_nop 0
	v_readlane_b32 s16, v68, 0
	s_nop 1
	v_cmp_gt_f32_e32 vcc, s16, v68
	v_cmp_eq_f32_e64 s[16:17], s16, v68
	s_and_b64 s[16:17], s[2:3], s[16:17]
	s_or_b64 s[16:17], vcc, s[16:17]
	v_cndmask_b32_e64 v69, 0, 1, s[16:17]
	v_readlane_b32 s16, v68, 8
	s_nop 1
	v_cmp_gt_f32_e32 vcc, s16, v68
	v_cmp_eq_f32_e64 s[16:17], s16, v68
	s_and_b64 s[16:17], s[4:5], s[16:17]
	s_or_b64 s[16:17], vcc, s[16:17]
	v_cndmask_b32_e64 v70, 0, 1, s[16:17]
	v_readlane_b32 s16, v68, 16
	s_nop 1
	v_cmp_gt_f32_e32 vcc, s16, v68
	v_cmp_eq_f32_e64 s[16:17], s16, v68
	s_and_b64 s[16:17], s[6:7], s[16:17]
	s_or_b64 s[16:17], vcc, s[16:17]
	v_cndmask_b32_e64 v71, 0, 1, s[16:17]
	v_readlane_b32 s16, v68, 24
	v_add3_u32 v69, v69, v70, v71
	s_nop 0
	v_cmp_gt_f32_e32 vcc, s16, v68
	v_cmp_eq_f32_e64 s[16:17], s16, v68
	s_and_b64 s[16:17], s[8:9], s[16:17]
	s_or_b64 s[16:17], vcc, s[16:17]
	v_cndmask_b32_e64 v70, 0, 1, s[16:17]
	v_readlane_b32 s16, v68, 32
	s_nop 1
	v_cmp_gt_f32_e32 vcc, s16, v68
	v_cmp_eq_f32_e64 s[16:17], s16, v68
	s_and_b64 s[16:17], s[10:11], s[16:17]
	s_or_b64 s[16:17], vcc, s[16:17]
	v_cndmask_b32_e64 v71, 0, 1, s[16:17]
	v_readlane_b32 s16, v68, 40
	v_add3_u32 v69, v69, v70, v71
	s_nop 0
	v_cmp_gt_f32_e32 vcc, s16, v68
	v_cmp_eq_f32_e64 s[16:17], s16, v68
	s_and_b64 s[16:17], s[12:13], s[16:17]
	s_or_b64 s[16:17], vcc, s[16:17]
	v_cndmask_b32_e64 v70, 0, 1, s[16:17]
	v_readlane_b32 s16, v68, 48
	s_nop 1
	v_cmp_gt_f32_e32 vcc, s16, v68
	v_cmp_eq_f32_e64 s[16:17], s16, v68
	s_and_b64 s[16:17], s[14:15], s[16:17]
	s_or_b64 s[16:17], vcc, s[16:17]
	v_cndmask_b32_e64 v71, 0, 1, s[16:17]
	v_readlane_b32 s16, v68, 56
	s_nop 1
	v_cmp_gt_f32_e32 vcc, s16, v68
	s_nop 1
	v_addc_co_u32_e32 v68, vcc, v69, v70, vcc
	v_add_u32_e32 v68, v68, v71
	v_cmp_gt_u32_e32 vcc, 4, v68
	s_nop 1
	v_cndmask_b32_e32 v67, v205, v67, vcc
	s_nop 1
	v_max_f32_dpp v68, v67, v67 quad_perm:[1,0,3,2] row_mask:0xf bank_mask:0xf
	s_nop 1
	v_max_f32_dpp v68, v68, v68 quad_perm:[2,3,0,1] row_mask:0xf bank_mask:0xf
	s_nop 1
	v_max_f32_dpp v68, v68, v68 row_half_mirror row_mask:0xf bank_mask:0xf
	s_nop 1
	v_max_f32_dpp v68, v68, v68 row_ror:8 row_mask:0xf bank_mask:0xf
	v_mov_b32_e32 v69, v68
	v_mov_b32_e32 v239, v68
	s_nop 1
	v_permlane16_swap_b32_e32 v69, v239
	v_max_f32_e32 v68, v69, v239
	v_mov_b32_e32 v69, v68
	v_mov_b32_e32 v239, v68
	s_nop 1
	v_permlane32_swap_b32_e32 v69, v239
	v_max_f32_e32 v68, v69, v239
	v_cmp_eq_f32_e32 vcc, v67, v68
	s_cmp_lg_u64 vcc, 0
	s_ff1_i32_b64 s18, vcc
	s_cselect_b64 s[16:17], -1, 0
	v_cmp_eq_u32_e32 vcc, s18, v206
	s_and_b64 vcc, s[16:17], vcc
	s_nop 0
	v_cndmask_b32_e32 v67, v67, v205, vcc
	s_nop 1
	v_max_f32_dpp v68, v67, v67 quad_perm:[1,0,3,2] row_mask:0xf bank_mask:0xf
	s_nop 1
	v_max_f32_dpp v68, v68, v68 quad_perm:[2,3,0,1] row_mask:0xf bank_mask:0xf
	s_nop 1
	v_max_f32_dpp v68, v68, v68 row_half_mirror row_mask:0xf bank_mask:0xf
	s_nop 1
	v_max_f32_dpp v68, v68, v68 row_ror:8 row_mask:0xf bank_mask:0xf
	v_mov_b32_e32 v69, v68
	v_mov_b32_e32 v239, v68
	s_nop 1
	v_permlane16_swap_b32_e32 v69, v239
	v_max_f32_e32 v68, v69, v239
	v_mov_b32_e32 v69, v68
	v_mov_b32_e32 v239, v68
	s_nop 1
	v_permlane32_swap_b32_e32 v69, v239
	v_max_f32_e32 v68, v69, v239
	v_cmp_eq_f32_e64 s[16:17], v67, v68
	s_cmp_lg_u64 s[16:17], 0
	s_ff1_i32_b64 s16, s[16:17]
	s_cselect_b64 s[18:19], -1, 0
	v_cmp_eq_u32_e64 s[16:17], s16, v206
	s_and_b64 s[16:17], s[18:19], s[16:17]
	s_nop 0
	v_cndmask_b32_e64 v67, v67, v205, s[16:17]
	s_nop 1
	v_max_f32_dpp v68, v67, v67 quad_perm:[1,0,3,2] row_mask:0xf bank_mask:0xf
	s_nop 1
	v_max_f32_dpp v68, v68, v68 quad_perm:[2,3,0,1] row_mask:0xf bank_mask:0xf
	s_nop 1
	v_max_f32_dpp v68, v68, v68 row_half_mirror row_mask:0xf bank_mask:0xf
	s_nop 1
	v_max_f32_dpp v68, v68, v68 row_ror:8 row_mask:0xf bank_mask:0xf
	v_mov_b32_e32 v69, v68
	v_mov_b32_e32 v239, v68
	s_nop 1
	v_permlane16_swap_b32_e32 v69, v239
	v_max_f32_e32 v68, v69, v239
	v_mov_b32_e32 v69, v68
	v_mov_b32_e32 v239, v68
	s_nop 1
	v_permlane32_swap_b32_e32 v69, v239
	v_max_f32_e32 v68, v69, v239
	v_cmp_eq_f32_e64 s[18:19], v67, v68
	s_cmp_lg_u64 s[18:19], 0
	s_ff1_i32_b64 s18, s[18:19]
	s_cselect_b64 s[20:21], -1, 0
	v_cmp_eq_u32_e64 s[18:19], s18, v206
	s_and_b64 s[18:19], s[20:21], s[18:19]
	s_nop 0
	v_cndmask_b32_e64 v67, v67, v205, s[18:19]
	s_nop 1
	v_max_f32_dpp v68, v67, v67 quad_perm:[1,0,3,2] row_mask:0xf bank_mask:0xf
	s_nop 1
	v_max_f32_dpp v68, v68, v68 quad_perm:[2,3,0,1] row_mask:0xf bank_mask:0xf
	s_nop 1
	v_max_f32_dpp v68, v68, v68 row_half_mirror row_mask:0xf bank_mask:0xf
	s_nop 1
	v_max_f32_dpp v68, v68, v68 row_ror:8 row_mask:0xf bank_mask:0xf
	v_mov_b32_e32 v69, v68
	v_mov_b32_e32 v239, v68
	s_nop 1
	v_permlane16_swap_b32_e32 v69, v239
	v_max_f32_e32 v68, v69, v239
	v_mov_b32_e32 v69, v68
	v_mov_b32_e32 v239, v68
	s_nop 1
	v_permlane32_swap_b32_e32 v69, v239
	v_max_f32_e32 v68, v69, v239
	v_cmp_eq_f32_e64 s[20:21], v67, v68
	s_cmp_lg_u64 s[20:21], 0
	s_ff1_i32_b64 s20, s[20:21]
	s_cselect_b64 s[22:23], -1, 0
	v_cmp_eq_u32_e64 s[20:21], s20, v206
	s_and_b64 s[20:21], s[22:23], s[20:21]
	s_nop 0
	v_cndmask_b32_e64 v67, v67, v205, s[20:21]
	s_nop 1
	v_max_f32_dpp v68, v67, v67 quad_perm:[1,0,3,2] row_mask:0xf bank_mask:0xf
	s_nop 1
	v_max_f32_dpp v68, v68, v68 quad_perm:[2,3,0,1] row_mask:0xf bank_mask:0xf
	s_nop 1
	v_max_f32_dpp v68, v68, v68 row_half_mirror row_mask:0xf bank_mask:0xf
	s_nop 1
	v_max_f32_dpp v68, v68, v68 row_ror:8 row_mask:0xf bank_mask:0xf
	v_mov_b32_e32 v69, v68
	v_mov_b32_e32 v239, v68
	s_nop 1
	v_permlane16_swap_b32_e32 v69, v239
	v_max_f32_e32 v68, v69, v239
	v_mov_b32_e32 v69, v68
	v_mov_b32_e32 v239, v68
	s_nop 1
	v_permlane32_swap_b32_e32 v69, v239
	v_max_f32_e32 v68, v69, v239
	v_cmp_eq_f32_e64 s[22:23], v67, v68
	s_cmp_lg_u64 s[22:23], 0
	s_ff1_i32_b64 s22, s[22:23]
	s_cselect_b64 s[24:25], -1, 0
	v_cmp_eq_u32_e64 s[22:23], s22, v206
	s_and_b64 s[22:23], s[24:25], s[22:23]
	s_nop 0
	v_cndmask_b32_e64 v67, v67, v205, s[22:23]
	v_max_f32_e32 v69, v67, v67
	s_nop 1
	v_max_f32_dpp v68, v67, v69 quad_perm:[1,0,3,2] row_mask:0xf bank_mask:0xf
	s_nop 1
	v_max_f32_dpp v68, v68, v68 quad_perm:[2,3,0,1] row_mask:0xf bank_mask:0xf
	s_nop 1
	v_max_f32_dpp v68, v68, v68 row_half_mirror row_mask:0xf bank_mask:0xf
	s_nop 1
	v_max_f32_dpp v68, v68, v68 row_ror:8 row_mask:0xf bank_mask:0xf
	v_mov_b32_e32 v69, v68
	v_mov_b32_e32 v239, v68
	s_nop 1
	v_permlane16_swap_b32_e32 v69, v239
	v_max_f32_e32 v68, v69, v239
	v_mov_b32_e32 v69, v68
	v_mov_b32_e32 v239, v68
	s_nop 1
	v_permlane32_swap_b32_e32 v69, v239
	v_max_f32_e32 v68, v69, v239
	v_cmp_eq_f32_e64 s[24:25], v67, v68
	s_cmp_lg_u64 s[24:25], 0
	s_ff1_i32_b64 s24, s[24:25]
	s_cselect_b64 s[26:27], -1, 0
	v_cmp_eq_u32_e64 s[24:25], s24, v206
	s_and_b64 s[24:25], s[26:27], s[24:25]
	s_nop 0
	v_cndmask_b32_e64 v67, v67, v205, s[24:25]
	v_max_f32_e32 v69, v67, v67
	s_nop 1
	v_max_f32_dpp v68, v67, v69 quad_perm:[1,0,3,2] row_mask:0xf bank_mask:0xf
	s_nop 1
	v_max_f32_dpp v68, v68, v68 quad_perm:[2,3,0,1] row_mask:0xf bank_mask:0xf
	s_nop 1
	v_max_f32_dpp v68, v68, v68 row_half_mirror row_mask:0xf bank_mask:0xf
	s_nop 1
	v_max_f32_dpp v68, v68, v68 row_ror:8 row_mask:0xf bank_mask:0xf
	v_mov_b32_e32 v69, v68
	v_mov_b32_e32 v239, v68
	s_nop 1
	v_permlane16_swap_b32_e32 v69, v239
	v_max_f32_e32 v68, v69, v239
	v_mov_b32_e32 v69, v68
	v_mov_b32_e32 v239, v68
	s_nop 1
	v_permlane32_swap_b32_e32 v69, v239
	v_max_f32_e32 v68, v69, v239
	v_cmp_eq_f32_e64 s[26:27], v67, v68
	s_cmp_lg_u64 s[26:27], 0
	s_ff1_i32_b64 s26, s[26:27]
	s_cselect_b64 s[28:29], -1, 0
	v_cmp_eq_u32_e64 s[26:27], s26, v206
	s_and_b64 s[26:27], s[28:29], s[26:27]
	s_nop 0
	v_cndmask_b32_e64 v67, v67, v205, s[26:27]
	v_max_f32_e32 v69, v67, v67
	s_nop 1
	v_max_f32_dpp v68, v67, v69 quad_perm:[1,0,3,2] row_mask:0xf bank_mask:0xf
	s_nop 1
	v_max_f32_dpp v68, v68, v68 quad_perm:[2,3,0,1] row_mask:0xf bank_mask:0xf
	s_nop 1
	v_max_f32_dpp v68, v68, v68 row_half_mirror row_mask:0xf bank_mask:0xf
	s_nop 1
	v_max_f32_dpp v68, v68, v68 row_ror:8 row_mask:0xf bank_mask:0xf
	v_mov_b32_e32 v69, v68
	v_mov_b32_e32 v239, v68
	s_nop 1
	v_permlane16_swap_b32_e32 v69, v239
	v_max_f32_e32 v68, v69, v239
	v_mov_b32_e32 v69, v68
	v_mov_b32_e32 v239, v68
	s_nop 1
	v_permlane32_swap_b32_e32 v69, v239
	v_max_f32_e32 v68, v69, v239
	v_cmp_eq_f32_e64 s[28:29], v67, v68
	s_cmp_lg_u64 s[28:29], 0
	s_ff1_i32_b64 s28, s[28:29]
	s_cselect_b64 s[76:77], -1, 0
	v_cmp_eq_u32_e64 s[28:29], s28, v206
	s_and_b64 s[28:29], s[76:77], s[28:29]
	s_or_b64 s[26:27], s[28:29], s[26:27]
	s_or_b64 s[24:25], s[26:27], s[24:25]
	s_or_b64 s[22:23], s[24:25], s[22:23]
	s_or_b64 s[20:21], s[22:23], s[20:21]
	s_or_b64 s[18:19], s[20:21], s[18:19]
	s_or_b64 s[16:17], s[18:19], s[16:17]
	s_or_b64 s[16:17], s[16:17], vcc
	v_cndmask_b32_e64 v67, 0, v66, s[16:17]
	v_cndmask_b32_e64 v69, 0, 1, s[16:17]
	v_cmp_ne_u32_e32 vcc, 0, v69
	s_nop 1
	v_add_f32_dpp v67, v67, v67 quad_perm:[1,0,3,2] row_mask:0xf bank_mask:0xf
	s_nop 1
	v_add_f32_dpp v67, v67, v67 quad_perm:[2,3,0,1] row_mask:0xf bank_mask:0xf
	s_nop 1
	v_add_f32_dpp v67, v67, v67 row_half_mirror row_mask:0xf bank_mask:0xf
	s_nop 1
	v_add_f32_dpp v67, v67, v67 row_ror:8 row_mask:0xf bank_mask:0xf
	v_mov_b32_e32 v68, v67
	v_mov_b32_e32 v239, v67
	s_nop 1
	v_permlane16_swap_b32_e32 v68, v239
	v_add_f32_e32 v67, v68, v239
	v_mov_b32_e32 v68, v67
	v_mov_b32_e32 v239, v67
	s_nop 1
	v_permlane32_swap_b32_e32 v68, v239
	v_cndmask_b32_e64 v68, v239, v68, s[100:101]
	s_and_saveexec_b64 s[18:19], s[16:17]
	s_cbranch_execz .LBB0_1142
	s_add_i32 s74, s74, s63
	s_cmpk_gt_i32 s74, 0x3fff
	s_waitcnt lgkmcnt(0)
	v_add_f32_e32 v67, v67, v68
	v_mbcnt_lo_u32_b32 v68, vcc_lo, 0
	s_cselect_b32 s16, 0x100, 0
	v_mbcnt_hi_u32_b32 v68, vcc_hi, v68
	v_add_u32_e32 v69, s16, v115
	ds_add_rtn_u32 v72, v69, v201
	v_lshl_add_u32 v68, s74, 3, v68
	v_div_scale_f32 v73, s[16:17], v67, v67, v66
	v_ashrrev_i32_e32 v69, 31, v68
	v_rcp_f32_e32 v116, v73
	v_lshlrev_b64 v[68:69], 2, v[68:69]
	v_lshl_add_u64 v[70:71], s[36:37], 0, v[68:69]
	global_store_dword v[70:71], v206, off
	v_lshl_add_u64 v[70:71], s[38:39], 0, v[68:69]
	s_waitcnt lgkmcnt(0)
	global_store_dword v[70:71], v72, off
	v_fma_f32 v70, -v73, v116, 1.0
	v_fmac_f32_e32 v116, v70, v116
	v_div_scale_f32 v70, vcc, v66, v67, v66
	v_mul_f32_e32 v71, v70, v116
	v_fma_f32 v72, -v73, v71, v70
	v_fmac_f32_e32 v71, v72, v116
	v_fma_f32 v70, -v73, v71, v70
	v_div_fmas_f32 v70, v70, v116, v71
	v_div_fixup_f32 v66, v70, v67, v66
	v_mul_f32_e32 v70, 0x40200000, v66
	v_lshl_add_u64 v[66:67], s[40:41], 0, v[68:69]
	global_store_dword v[66:67], v70, off
	s_branch .LBB0_1142
